# v3 + fill_rowtab gather-row loads issued together (one wait) instead of ten serialized load-wait pairs
# speedup vs baseline: 1.0009x; 1.0009x over previous
.LBB0_662:
	s_or_b64 exec, exec, s[4:5]
	s_add_u32 s12, s90, 0x100000
	s_addc_u32 s13, s91, 0
	s_add_i32 s0, 0, 0x20600
	v_mov_b32_e32 v0, s0
	s_waitcnt lgkmcnt(0)
	s_barrier
	ds_read_b32 v0, v0
	v_readlane_b32 s0, v255, 4
	s_mov_b32 s27, 0
	s_waitcnt lgkmcnt(0)
	v_readfirstlane_b32 s3, v0
	v_mbcnt_lo_u32_b32 v0, -1, 0
	v_mbcnt_hi_u32_b32 v0, -1, v0
	s_lshl_b32 s48, s3, 4
	v_add_u32_e32 v0, s0, v0
	s_movk_i32 s0, 0x100
	s_nop 0
	v_cmp_gt_i32_e32 vcc, s0, v0
	s_and_saveexec_b64 s[0:1], vcc
	s_cbranch_execz .LBB0_763
	s_cmp_ge_i32 s60, s48
	s_cbranch_scc1 .LBB0_763
	v_mov_b32_e32 v10, 0
	v_mov_b32_e32 v11, 0
	v_mov_b32_e32 v12, 0
	v_mov_b32_e32 v13, 0
	v_mov_b32_e32 v14, 0
	v_mov_b32_e32 v15, 0
	v_mov_b32_e32 v16, 0
	v_mov_b32_e32 v17, 0
	v_mov_b32_e32 v18, 0
	v_mov_b32_e32 v19, 0
	s_ashr_i32 s4, s60, 31
	s_lshr_b32 s4, s4, 29
	s_add_i32 s4, s60, s4
	s_lshl_b32 s2, s3, 1
	s_ashr_i32 s5, s4, 3
	s_and_b32 s4, s4, -8
	s_or_b32 s6, s2, 1
	s_sub_i32 s4, s60, s4
	s_cmp_lt_i32 s4, 0
	s_cselect_b32 s14, s6, s2
	s_add_i32 s7, 0, 0x20584
	v_mov_b32_e32 v1, s7
	ds_read_b32 v1, v1
	s_mul_i32 s4, s4, s14
	s_add_i32 s4, s4, s5
	s_mov_b32 s7, 1
	s_mov_b32 s16, 0
	s_waitcnt lgkmcnt(0)
	v_readfirstlane_b32 s5, v1
	s_lshl_b32 s5, s5, 4
	s_cmp_lt_i32 s4, s5
	s_cbranch_scc1 .LBB0_697
	s_add_i32 s5, 0, 0x20588
	v_mov_b32_e32 v1, s5
	ds_read_b32 v1, v1
	s_waitcnt lgkmcnt(0)
	v_readfirstlane_b32 s5, v1
	s_lshl_b32 s5, s5, 4
	s_cmp_lt_i32 s4, s5
	s_cbranch_scc1 .LBB0_696
	s_add_i32 s5, 0, 0x2058c
	v_mov_b32_e32 v1, s5
	ds_read_b32 v1, v1
	s_mov_b32 s7, 2
	s_waitcnt lgkmcnt(0)
	v_readfirstlane_b32 s5, v1
	s_lshl_b32 s5, s5, 4
	s_cmp_lt_i32 s4, s5
	s_cbranch_scc1 .LBB0_696
	s_add_i32 s5, 0, 0x20590
	v_mov_b32_e32 v1, s5
	ds_read_b32 v1, v1
	s_mov_b32 s7, 3
	s_waitcnt lgkmcnt(0)
	v_readfirstlane_b32 s5, v1
	s_lshl_b32 s5, s5, 4
	s_cmp_lt_i32 s4, s5
	s_cbranch_scc1 .LBB0_696
	s_add_i32 s5, 0, 0x20594
	v_mov_b32_e32 v1, s5
	ds_read_b32 v1, v1
	s_mov_b32 s7, 4
	s_waitcnt lgkmcnt(0)
	v_readfirstlane_b32 s5, v1
	s_lshl_b32 s5, s5, 4
	s_cmp_lt_i32 s4, s5
	s_cbranch_scc1 .LBB0_696
	s_add_i32 s5, 0, 0x20598
	v_mov_b32_e32 v1, s5
	ds_read_b32 v1, v1
	s_mov_b32 s7, 5
	s_waitcnt lgkmcnt(0)
	v_readfirstlane_b32 s5, v1
	s_lshl_b32 s5, s5, 4
	s_cmp_lt_i32 s4, s5
	s_cbranch_scc1 .LBB0_696
	s_add_i32 s5, 0, 0x2059c
	v_mov_b32_e32 v1, s5
	ds_read_b32 v1, v1
	s_mov_b32 s7, 6
	s_waitcnt lgkmcnt(0)
	v_readfirstlane_b32 s5, v1
	s_lshl_b32 s5, s5, 4
	s_cmp_lt_i32 s4, s5
	s_cbranch_scc1 .LBB0_696
	s_add_i32 s5, 0, 0x205a0
	v_mov_b32_e32 v1, s5
	ds_read_b32 v1, v1
	s_mov_b32 s7, 7
	s_waitcnt lgkmcnt(0)
	v_readfirstlane_b32 s5, v1
	s_lshl_b32 s5, s5, 4
	s_cmp_lt_i32 s4, s5
	s_cbranch_scc1 .LBB0_696
	s_add_i32 s5, 0, 0x205a4
	v_mov_b32_e32 v1, s5
	ds_read_b32 v1, v1
	s_mov_b32 s7, 8
	s_waitcnt lgkmcnt(0)
	v_readfirstlane_b32 s5, v1
	s_lshl_b32 s5, s5, 4
	s_cmp_lt_i32 s4, s5
	s_cbranch_scc1 .LBB0_696
	s_add_i32 s5, 0, 0x205a8
	v_mov_b32_e32 v1, s5
	ds_read_b32 v1, v1
	s_mov_b32 s7, 9
	s_waitcnt lgkmcnt(0)
	v_readfirstlane_b32 s5, v1
	s_lshl_b32 s5, s5, 4
	s_cmp_lt_i32 s4, s5
	s_cbranch_scc1 .LBB0_696
	s_add_i32 s5, 0, 0x205ac
	v_mov_b32_e32 v1, s5
	ds_read_b32 v1, v1
	s_mov_b32 s7, 10
	s_waitcnt lgkmcnt(0)
	v_readfirstlane_b32 s5, v1
	s_lshl_b32 s5, s5, 4
	s_cmp_lt_i32 s4, s5
	s_cbranch_scc1 .LBB0_696
	s_add_i32 s5, 0, 0x205b0
	v_mov_b32_e32 v1, s5
	ds_read_b32 v1, v1
	s_mov_b32 s7, 11
	s_waitcnt lgkmcnt(0)
	v_readfirstlane_b32 s5, v1
	s_lshl_b32 s5, s5, 4
	s_cmp_lt_i32 s4, s5
	s_cbranch_scc1 .LBB0_696
	s_add_i32 s7, 0, 0x205b4
	v_mov_b32_e32 v1, s7
	ds_read_b32 v1, v1
	s_waitcnt lgkmcnt(0)
	v_readfirstlane_b32 s7, v1
	s_lshl_b32 s7, s7, 4
	s_cmp_lt_i32 s4, s7
	s_mov_b32 s7, 12
	s_cbranch_scc1 .LBB0_695
	s_add_i32 s7, 0, 0x205b8
	v_mov_b32_e32 v1, s7
	ds_read_b32 v1, v1
	s_waitcnt lgkmcnt(0)
	v_readfirstlane_b32 s7, v1
	s_lshl_b32 s7, s7, 4
	s_cmp_lt_i32 s4, s7
	s_mov_b32 s7, 13
	s_cbranch_scc1 .LBB0_695
	s_add_i32 s7, 0, 0x205bc
	v_mov_b32_e32 v1, s7
	ds_read_b32 v1, v1
	s_waitcnt lgkmcnt(0)
	v_readfirstlane_b32 s7, v1
	s_lshl_b32 s7, s7, 4
	s_cmp_lt_i32 s4, s7
	s_mov_b32 s7, 14
	s_cbranch_scc1 .LBB0_695
	s_add_i32 s7, 0, 0x205c0
	v_mov_b32_e32 v1, s7
	ds_read_b32 v1, v1
	s_waitcnt lgkmcnt(0)
	v_readfirstlane_b32 s7, v1
	s_lshl_b32 s7, s7, 4
	s_cmp_lt_i32 s4, s7
	s_mov_b32 s7, 15
	s_cbranch_scc1 .LBB0_695
	s_add_i32 s7, 0, 0x205c4
	v_mov_b32_e32 v1, s7
	ds_read_b32 v1, v1
	s_waitcnt lgkmcnt(0)
	v_readfirstlane_b32 s7, v1
	s_lshl_b32 s7, s7, 4
	s_cmp_lt_i32 s4, s7
	s_mov_b32 s7, 16
	s_cbranch_scc1 .LBB0_695
	s_add_i32 s7, 0, 0x205c8
	v_mov_b32_e32 v1, s7
	ds_read_b32 v1, v1
	s_waitcnt lgkmcnt(0)
	v_readfirstlane_b32 s7, v1
	s_lshl_b32 s7, s7, 4
	s_cmp_lt_i32 s4, s7
	s_mov_b32 s7, 17
	s_cbranch_scc1 .LBB0_695
	s_add_i32 s7, 0, 0x205cc
	v_mov_b32_e32 v1, s7
	ds_read_b32 v1, v1
	s_waitcnt lgkmcnt(0)
	v_readfirstlane_b32 s7, v1
	s_lshl_b32 s7, s7, 4
	s_cmp_lt_i32 s4, s7
	s_mov_b32 s7, 18
	s_cbranch_scc1 .LBB0_695
	s_add_i32 s7, 0, 0x205d0
	v_mov_b32_e32 v1, s7
	ds_read_b32 v1, v1
	s_waitcnt lgkmcnt(0)
	v_readfirstlane_b32 s7, v1
	s_lshl_b32 s7, s7, 4
	s_cmp_lt_i32 s4, s7
	s_mov_b32 s7, 19
	s_cbranch_scc1 .LBB0_695
	s_add_i32 s7, 0, 0x205d4
	v_mov_b32_e32 v1, s7
	ds_read_b32 v1, v1
	s_waitcnt lgkmcnt(0)
	v_readfirstlane_b32 s7, v1
	s_lshl_b32 s7, s7, 4
	s_cmp_lt_i32 s4, s7
	s_mov_b32 s7, 20
	s_cbranch_scc1 .LBB0_695
	s_add_i32 s7, 0, 0x205d8
	v_mov_b32_e32 v1, s7
	ds_read_b32 v1, v1
	s_waitcnt lgkmcnt(0)
	v_readfirstlane_b32 s7, v1
	s_lshl_b32 s7, s7, 4
	s_cmp_lt_i32 s4, s7
	s_mov_b32 s7, 21
	s_cbranch_scc1 .LBB0_695
	s_add_i32 s7, 0, 0x205dc
	v_mov_b32_e32 v1, s7
	ds_read_b32 v1, v1
	s_waitcnt lgkmcnt(0)
	v_readfirstlane_b32 s7, v1
	s_lshl_b32 s7, s7, 4
	s_cmp_lt_i32 s4, s7
	s_mov_b32 s7, 22
	s_cbranch_scc1 .LBB0_695
	s_add_i32 s7, 0, 0x205e0
	v_mov_b32_e32 v1, s7
	ds_read_b32 v1, v1
	s_waitcnt lgkmcnt(0)
	v_readfirstlane_b32 s7, v1
	s_lshl_b32 s7, s7, 4
	s_cmp_lt_i32 s4, s7
	s_mov_b32 s7, 23
	s_cbranch_scc1 .LBB0_695
	s_add_i32 s7, 0, 0x205e4
	v_mov_b32_e32 v1, s7
	ds_read_b32 v1, v1
	s_waitcnt lgkmcnt(0)
	v_readfirstlane_b32 s7, v1
	s_lshl_b32 s7, s7, 4
	s_cmp_lt_i32 s4, s7
	s_mov_b32 s7, 24
	s_cbranch_scc1 .LBB0_695
	s_add_i32 s7, 0, 0x205e8
	v_mov_b32_e32 v1, s7
	ds_read_b32 v1, v1
	s_waitcnt lgkmcnt(0)
	v_readfirstlane_b32 s7, v1
	s_lshl_b32 s7, s7, 4
	s_cmp_lt_i32 s4, s7
	s_mov_b32 s7, 25
	s_cbranch_scc1 .LBB0_695
	s_add_i32 s7, 0, 0x205ec
	v_mov_b32_e32 v1, s7
	ds_read_b32 v1, v1
	s_waitcnt lgkmcnt(0)
	v_readfirstlane_b32 s7, v1
	s_lshl_b32 s7, s7, 4
	s_cmp_lt_i32 s4, s7
	s_mov_b32 s7, 26
	s_cbranch_scc1 .LBB0_695
	s_add_i32 s7, 0, 0x205f0
	v_mov_b32_e32 v1, s7
	ds_read_b32 v1, v1
	s_waitcnt lgkmcnt(0)
	v_readfirstlane_b32 s7, v1
	s_lshl_b32 s7, s7, 4
	s_cmp_lt_i32 s4, s7
	s_mov_b32 s7, 27
	s_cbranch_scc1 .LBB0_695
	s_add_i32 s7, 0, 0x205f4
	v_mov_b32_e32 v1, s7
	ds_read_b32 v1, v1
	s_waitcnt lgkmcnt(0)
	v_readfirstlane_b32 s7, v1
	s_lshl_b32 s7, s7, 4
	s_cmp_lt_i32 s4, s7
	s_mov_b32 s7, 28
	s_cbranch_scc1 .LBB0_695
	s_add_i32 s7, 0, 0x205f8
	v_mov_b32_e32 v1, s7
	ds_read_b32 v1, v1
	s_waitcnt lgkmcnt(0)
	v_readfirstlane_b32 s7, v1
	s_lshl_b32 s7, s7, 4
	s_cmp_lt_i32 s4, s7
	s_mov_b32 s7, 29
	s_cbranch_scc1 .LBB0_695
	s_add_i32 s7, 0, 0x205fc
	v_mov_b32_e32 v1, s7
	ds_read_b32 v1, v1
	s_waitcnt lgkmcnt(0)
	v_readfirstlane_b32 s7, v1
	s_lshl_b32 s7, s7, 4
	s_cmp_lt_i32 s4, s7
	s_cselect_b32 s7, 30, 31

.LBB0_697:
	s_lshl_b32 s5, s16, 2
	s_add_i32 s7, s5, 0
	s_add_i32 s5, s7, 0x20400
	v_mov_b32_e32 v1, s5
	ds_read2_b32 v[2:3], v1 offset1:32
	ds_read_b32 v1, v1 offset:384
	s_waitcnt lgkmcnt(1)
	v_readfirstlane_b32 s5, v3
	s_abs_i32 s5, s5
	s_nop 0
	v_cvt_f32_u32_e32 v3, s5
	s_waitcnt lgkmcnt(0)
	v_readfirstlane_b32 s14, v1
	s_lshl_b32 s14, s14, 4
	s_sub_i32 s4, s4, s14
	v_rcp_iflag_f32_e32 v1, v3
	s_sub_i32 s14, 0, s5
	s_ashr_i32 s17, s4, 31
	s_abs_i32 s4, s4
	v_mul_f32_e32 v1, 0x4f7ffffe, v1
	v_cvt_u32_f32_e32 v1, v1
	v_readfirstlane_b32 s15, v2
	v_mov_b32_e32 v2, 0
	v_readfirstlane_b32 s18, v1
	s_mul_i32 s14, s14, s18
	s_mul_hi_u32 s14, s18, s14
	s_add_i32 s18, s18, s14
	s_mul_hi_u32 s14, s4, s18
	s_mul_i32 s14, s14, s5
	s_sub_i32 s4, s4, s14
	s_sub_i32 s14, s4, s5
	s_cmp_ge_u32 s4, s5
	s_cselect_b32 s4, s14, s4
	s_sub_i32 s14, s4, s5
	s_cmp_ge_u32 s4, s5
	s_cselect_b32 s4, s14, s4
	s_xor_b32 s4, s4, s17
	s_sub_i32 s4, s4, s17
	s_lshl_b32 s5, s16, 13
	s_lshl_b32 s4, s4, 8
	s_add_i32 s14, s4, s5
	s_sub_i32 s4, s15, s4
	v_cmp_gt_i32_e32 vcc, s4, v0
	v_mov_b32_e32 v10, 0
	s_and_saveexec_b64 s[4:5], vcc
	s_cbranch_execz .LBB0_699
	v_add_u32_e32 v2, s14, v0
	v_ashrrev_i32_e32 v3, 31, v2
	v_lshl_add_u64 v[2:3], v[2:3], 2, s[12:13]
	global_load_dword v10, v[2:3], off
.LBB0_699:
	s_or_b64 exec, exec, s[4:5]
	v_lshl_add_u32 v1, v0, 2, 0
	s_add_i32 s14, s70, s60
	v_add_u32_e32 v1, 0x24000, v1
	s_cmp_ge_i32 s14, s48
	s_cbranch_scc1 .Lrt_fin
	s_ashr_i32 s4, s14, 31
	s_lshr_b32 s4, s4, 29
	s_add_i32 s4, s14, s4
	s_ashr_i32 s5, s4, 3
	s_and_b32 s4, s4, -8
	s_sub_i32 s4, s14, s4
	s_cmp_lt_i32 s4, 0
	s_cselect_b32 s15, s6, s2
	s_mul_i32 s17, s4, s15
	s_add_i32 s17, s17, s5
	s_add_i32 s18, s7, 0x20584
	s_branch .LBB0_702

.LBB0_704:
	s_lshl_b32 s4, s15, 2
	s_add_i32 s4, s4, 0
	s_add_i32 s4, s4, 0x20400
	s_waitcnt vmcnt(10)
	v_mov_b32_e32 v4, s4
	ds_read2_b32 v[2:3], v4 offset1:32
	ds_read_b32 v4, v4 offset:384
	s_waitcnt lgkmcnt(1)
	v_readfirstlane_b32 s4, v3
	s_abs_i32 s4, s4
	s_nop 0
	v_cvt_f32_u32_e32 v3, s4
	v_readfirstlane_b32 s18, v2
	s_waitcnt lgkmcnt(0)
	v_readfirstlane_b32 s5, v4
	s_sub_i32 s16, 0, s4
	v_rcp_iflag_f32_e32 v3, v3
	s_lshl_b32 s5, s5, 4
	s_sub_i32 s5, s17, s5
	s_ashr_i32 s17, s5, 31
	v_mul_f32_e32 v2, 0x4f7ffffe, v3
	v_cvt_u32_f32_e32 v2, v2
	s_abs_i32 s5, s5
	v_readfirstlane_b32 s19, v2
	s_mul_i32 s16, s16, s19
	s_mul_hi_u32 s16, s19, s16
	s_add_i32 s19, s19, s16
	s_mul_hi_u32 s16, s5, s19
	s_mul_i32 s16, s16, s4
	s_sub_i32 s5, s5, s16
	s_sub_i32 s16, s5, s4
	s_cmp_ge_u32 s5, s4
	s_cselect_b32 s5, s16, s5
	s_sub_i32 s16, s5, s4
	s_cmp_ge_u32 s5, s4
	s_cselect_b32 s4, s16, s5
	s_xor_b32 s4, s4, s17
	s_sub_i32 s4, s4, s17
	s_lshl_b32 s5, s15, 13
	s_lshl_b32 s4, s4, 8
	s_add_i32 s16, s4, s5
	s_sub_i32 s4, s18, s4
	v_cmp_gt_i32_e32 vcc, s4, v0
	v_mov_b32_e32 v2, 0
	v_mov_b32_e32 v11, 0
	s_and_saveexec_b64 s[4:5], vcc
	s_cbranch_execz .LBB0_706
	v_add_u32_e32 v2, s16, v0
	v_ashrrev_i32_e32 v3, 31, v2
	v_lshl_add_u64 v[2:3], v[2:3], 2, s[12:13]
	global_load_dword v11, v[2:3], off
.LBB0_706:
	s_or_b64 exec, exec, s[4:5]
	s_add_i32 s16, s14, s70
	s_cmp_ge_i32 s16, s48
	s_cbranch_scc1 .Lrt_fin
	s_ashr_i32 s4, s16, 31
	s_lshr_b32 s4, s4, 29
	s_add_i32 s4, s16, s4
	s_ashr_i32 s5, s4, 3
	s_and_b32 s4, s4, -8
	s_sub_i32 s4, s16, s4
	s_cmp_lt_i32 s4, 0
	s_cselect_b32 s14, s6, s2
	s_mul_i32 s18, s4, s14
	s_add_i32 s18, s18, s5
	s_branch .LBB0_709

.LBB0_711:
	s_lshl_b32 s4, s14, 2
	s_add_i32 s4, s4, 0
	s_add_i32 s4, s4, 0x20400
	v_mov_b32_e32 v4, s4
	ds_read2_b32 v[2:3], v4 offset1:32
	ds_read_b32 v4, v4 offset:384
	s_waitcnt lgkmcnt(1)
	v_readfirstlane_b32 s4, v3
	s_abs_i32 s4, s4
	s_nop 0
	v_cvt_f32_u32_e32 v3, s4
	v_readfirstlane_b32 s15, v2
	s_waitcnt lgkmcnt(0)
	v_readfirstlane_b32 s5, v4
	s_sub_i32 s7, 0, s4
	v_rcp_iflag_f32_e32 v3, v3
	s_lshl_b32 s5, s5, 4
	s_sub_i32 s5, s18, s5
	s_ashr_i32 s18, s5, 31
	v_mul_f32_e32 v2, 0x4f7ffffe, v3
	v_cvt_u32_f32_e32 v2, v2
	s_abs_i32 s5, s5
	v_readfirstlane_b32 s19, v2
	s_mul_i32 s7, s7, s19
	s_mul_hi_u32 s7, s19, s7
	s_add_i32 s19, s19, s7
	s_mul_hi_u32 s7, s5, s19
	s_mul_i32 s7, s7, s4
	s_sub_i32 s5, s5, s7
	s_sub_i32 s7, s5, s4
	s_cmp_ge_u32 s5, s4
	s_cselect_b32 s5, s7, s5
	s_sub_i32 s7, s5, s4
	s_cmp_ge_u32 s5, s4
	s_cselect_b32 s4, s7, s5
	s_xor_b32 s4, s4, s18
	s_sub_i32 s4, s4, s18
	s_lshl_b32 s5, s14, 13
	s_lshl_b32 s4, s4, 8
	s_add_i32 s7, s4, s5
	s_sub_i32 s4, s15, s4
	v_cmp_gt_i32_e32 vcc, s4, v0
	v_mov_b32_e32 v2, 0
	v_mov_b32_e32 v12, 0
	s_and_saveexec_b64 s[4:5], vcc
	s_cbranch_execz .LBB0_713
	v_add_u32_e32 v2, s7, v0
	v_ashrrev_i32_e32 v3, 31, v2
	v_lshl_add_u64 v[2:3], v[2:3], 2, s[12:13]
	global_load_dword v12, v[2:3], off
.LBB0_713:
	s_or_b64 exec, exec, s[4:5]
	s_add_i32 s15, s16, s70
	s_cmp_ge_i32 s15, s48
	s_cbranch_scc1 .Lrt_fin
	s_ashr_i32 s4, s15, 31
	s_lshr_b32 s4, s4, 29
	s_add_i32 s4, s15, s4
	s_ashr_i32 s5, s4, 3
	s_and_b32 s4, s4, -8
	s_sub_i32 s4, s15, s4
	s_cmp_lt_i32 s4, 0
	s_cselect_b32 s7, s6, s2
	s_mul_i32 s18, s4, s7
	s_min_u32 s4, s17, 31
	s_lshl_b32 s4, s4, 2
	s_add_i32 s4, s4, 0
	s_add_i32 s18, s18, s5
	s_add_i32 s17, s4, 0x20584
	s_branch .LBB0_716

.LBB0_718:
	s_lshl_b32 s4, s7, 2
	s_add_i32 s4, s4, 0
	s_add_i32 s4, s4, 0x20400
	v_mov_b32_e32 v4, s4
	ds_read2_b32 v[2:3], v4 offset1:32
	ds_read_b32 v4, v4 offset:384
	s_waitcnt lgkmcnt(1)
	v_readfirstlane_b32 s4, v3
	s_abs_i32 s4, s4
	s_nop 0
	v_cvt_f32_u32_e32 v3, s4
	v_readfirstlane_b32 s17, v2
	s_waitcnt lgkmcnt(0)
	v_readfirstlane_b32 s5, v4
	s_sub_i32 s14, 0, s4
	v_rcp_iflag_f32_e32 v3, v3
	s_lshl_b32 s5, s5, 4
	s_sub_i32 s5, s18, s5
	s_ashr_i32 s18, s5, 31
	v_mul_f32_e32 v2, 0x4f7ffffe, v3
	v_cvt_u32_f32_e32 v2, v2
	s_abs_i32 s5, s5
	v_readfirstlane_b32 s19, v2
	s_mul_i32 s14, s14, s19
	s_mul_hi_u32 s14, s19, s14
	s_add_i32 s19, s19, s14
	s_mul_hi_u32 s14, s5, s19
	s_mul_i32 s14, s14, s4
	s_sub_i32 s5, s5, s14
	s_sub_i32 s14, s5, s4
	s_cmp_ge_u32 s5, s4
	s_cselect_b32 s5, s14, s5
	s_sub_i32 s14, s5, s4
	s_cmp_ge_u32 s5, s4
	s_cselect_b32 s4, s14, s5
	s_xor_b32 s4, s4, s18
	s_sub_i32 s4, s4, s18
	s_lshl_b32 s5, s7, 13
	s_lshl_b32 s4, s4, 8
	s_add_i32 s14, s4, s5
	s_sub_i32 s4, s17, s4
	v_cmp_gt_i32_e32 vcc, s4, v0
	v_mov_b32_e32 v2, 0
	v_mov_b32_e32 v13, 0
	s_and_saveexec_b64 s[4:5], vcc
	s_cbranch_execz .LBB0_720
	v_add_u32_e32 v2, s14, v0
	v_ashrrev_i32_e32 v3, 31, v2
	v_lshl_add_u64 v[2:3], v[2:3], 2, s[12:13]
	global_load_dword v13, v[2:3], off
.LBB0_720:
	s_or_b64 exec, exec, s[4:5]
	s_add_i32 s15, s15, s70
	s_cmp_ge_i32 s15, s48
	s_cbranch_scc1 .Lrt_fin
	s_ashr_i32 s4, s15, 31
	s_lshr_b32 s4, s4, 29
	s_add_i32 s4, s15, s4
	s_ashr_i32 s5, s4, 3
	s_and_b32 s4, s4, -8
	s_sub_i32 s4, s15, s4
	s_cmp_lt_i32 s4, 0
	s_cselect_b32 s14, s6, s2
	s_mul_i32 s17, s4, s14
	s_min_u32 s4, s16, 31
	s_lshl_b32 s4, s4, 2
	s_add_i32 s4, s4, 0
	s_add_i32 s17, s17, s5
	s_add_i32 s18, s4, 0x20584
	s_branch .LBB0_723

.LBB0_725:
	s_lshl_b32 s4, s14, 2
	s_add_i32 s4, s4, 0
	s_add_i32 s4, s4, 0x20400
	v_mov_b32_e32 v4, s4
	ds_read2_b32 v[2:3], v4 offset1:32
	ds_read_b32 v4, v4 offset:384
	s_waitcnt lgkmcnt(1)
	v_readfirstlane_b32 s4, v3
	s_abs_i32 s4, s4
	s_nop 0
	v_cvt_f32_u32_e32 v3, s4
	v_readfirstlane_b32 s18, v2
	s_waitcnt lgkmcnt(0)
	v_readfirstlane_b32 s5, v4
	s_sub_i32 s7, 0, s4
	v_rcp_iflag_f32_e32 v3, v3
	s_lshl_b32 s5, s5, 4
	s_sub_i32 s5, s17, s5
	s_ashr_i32 s17, s5, 31
	v_mul_f32_e32 v2, 0x4f7ffffe, v3
	v_cvt_u32_f32_e32 v2, v2
	s_abs_i32 s5, s5
	v_readfirstlane_b32 s19, v2
	s_mul_i32 s7, s7, s19
	s_mul_hi_u32 s7, s19, s7
	s_add_i32 s19, s19, s7
	s_mul_hi_u32 s7, s5, s19
	s_mul_i32 s7, s7, s4
	s_sub_i32 s5, s5, s7
	s_sub_i32 s7, s5, s4
	s_cmp_ge_u32 s5, s4
	s_cselect_b32 s5, s7, s5
	s_sub_i32 s7, s5, s4
	s_cmp_ge_u32 s5, s4
	s_cselect_b32 s4, s7, s5
	s_xor_b32 s4, s4, s17
	s_sub_i32 s4, s4, s17
	s_lshl_b32 s5, s14, 13
	s_lshl_b32 s4, s4, 8
	s_add_i32 s7, s4, s5
	s_sub_i32 s4, s18, s4
	v_cmp_gt_i32_e32 vcc, s4, v0
	v_mov_b32_e32 v2, 0
	v_mov_b32_e32 v14, 0
	s_and_saveexec_b64 s[4:5], vcc
	s_cbranch_execz .LBB0_727
	v_add_u32_e32 v2, s7, v0
	v_ashrrev_i32_e32 v3, 31, v2
	v_lshl_add_u64 v[2:3], v[2:3], 2, s[12:13]
	global_load_dword v14, v[2:3], off
.LBB0_727:
	s_or_b64 exec, exec, s[4:5]
	s_add_i32 s15, s15, s70
	s_cmp_ge_i32 s15, s48
	s_cbranch_scc1 .Lrt_fin
	s_ashr_i32 s4, s15, 31
	s_lshr_b32 s4, s4, 29
	s_add_i32 s4, s15, s4
	s_ashr_i32 s5, s4, 3
	s_and_b32 s4, s4, -8
	s_sub_i32 s4, s15, s4
	s_cmp_lt_i32 s4, 0
	s_cselect_b32 s7, s6, s2
	s_mul_i32 s17, s4, s7
	s_min_u32 s4, s16, 31
	s_lshl_b32 s4, s4, 2
	s_add_i32 s4, s4, 0
	s_add_i32 s17, s17, s5
	s_add_i32 s18, s4, 0x20584
	s_branch .LBB0_730

.LBB0_732:
	s_lshl_b32 s4, s7, 2
	s_add_i32 s4, s4, 0
	s_add_i32 s4, s4, 0x20400
	v_mov_b32_e32 v4, s4
	ds_read2_b32 v[2:3], v4 offset1:32
	ds_read_b32 v4, v4 offset:384
	s_waitcnt lgkmcnt(1)
	v_readfirstlane_b32 s4, v3
	s_abs_i32 s4, s4
	s_nop 0
	v_cvt_f32_u32_e32 v3, s4
	v_readfirstlane_b32 s18, v2
	s_waitcnt lgkmcnt(0)
	v_readfirstlane_b32 s5, v4
	s_sub_i32 s14, 0, s4
	v_rcp_iflag_f32_e32 v3, v3
	s_lshl_b32 s5, s5, 4
	s_sub_i32 s5, s17, s5
	s_ashr_i32 s17, s5, 31
	v_mul_f32_e32 v2, 0x4f7ffffe, v3
	v_cvt_u32_f32_e32 v2, v2
	s_abs_i32 s5, s5
	v_readfirstlane_b32 s19, v2
	s_mul_i32 s14, s14, s19
	s_mul_hi_u32 s14, s19, s14
	s_add_i32 s19, s19, s14
	s_mul_hi_u32 s14, s5, s19
	s_mul_i32 s14, s14, s4
	s_sub_i32 s5, s5, s14
	s_sub_i32 s14, s5, s4
	s_cmp_ge_u32 s5, s4
	s_cselect_b32 s5, s14, s5
	s_sub_i32 s14, s5, s4
	s_cmp_ge_u32 s5, s4
	s_cselect_b32 s4, s14, s5
	s_xor_b32 s4, s4, s17
	s_sub_i32 s4, s4, s17
	s_lshl_b32 s5, s7, 13
	s_lshl_b32 s4, s4, 8
	s_add_i32 s14, s4, s5
	s_sub_i32 s4, s18, s4
	v_cmp_gt_i32_e32 vcc, s4, v0
	v_mov_b32_e32 v2, 0
	v_mov_b32_e32 v15, 0
	s_and_saveexec_b64 s[4:5], vcc
	s_cbranch_execz .LBB0_734
	v_add_u32_e32 v2, s14, v0
	v_ashrrev_i32_e32 v3, 31, v2
	v_lshl_add_u64 v[2:3], v[2:3], 2, s[12:13]
	global_load_dword v15, v[2:3], off

.LBB0_739:
	s_lshl_b32 s4, s14, 2
	s_add_i32 s4, s4, 0
	s_add_i32 s4, s4, 0x20400
	v_mov_b32_e32 v4, s4
	ds_read2_b32 v[2:3], v4 offset1:32
	ds_read_b32 v4, v4 offset:384
	s_waitcnt lgkmcnt(1)
	v_readfirstlane_b32 s4, v3
	s_abs_i32 s4, s4
	s_nop 0
	v_cvt_f32_u32_e32 v3, s4
	v_readfirstlane_b32 s18, v2
	s_waitcnt lgkmcnt(0)
	v_readfirstlane_b32 s5, v4
	s_sub_i32 s7, 0, s4
	v_rcp_iflag_f32_e32 v3, v3
	s_lshl_b32 s5, s5, 4
	s_sub_i32 s5, s17, s5
	s_ashr_i32 s17, s5, 31
	v_mul_f32_e32 v2, 0x4f7ffffe, v3
	v_cvt_u32_f32_e32 v2, v2
	s_abs_i32 s5, s5
	v_readfirstlane_b32 s19, v2
	s_mul_i32 s7, s7, s19
	s_mul_hi_u32 s7, s19, s7
	s_add_i32 s19, s19, s7
	s_mul_hi_u32 s7, s5, s19
	s_mul_i32 s7, s7, s4
	s_sub_i32 s5, s5, s7
	s_sub_i32 s7, s5, s4
	s_cmp_ge_u32 s5, s4
	s_cselect_b32 s5, s7, s5
	s_sub_i32 s7, s5, s4
	s_cmp_ge_u32 s5, s4
	s_cselect_b32 s4, s7, s5
	s_xor_b32 s4, s4, s17
	s_sub_i32 s4, s4, s17
	s_lshl_b32 s5, s14, 13
	s_lshl_b32 s4, s4, 8
	s_add_i32 s7, s4, s5
	s_sub_i32 s4, s18, s4
	v_cmp_gt_i32_e32 vcc, s4, v0
	v_mov_b32_e32 v2, 0
	v_mov_b32_e32 v16, 0
	s_and_saveexec_b64 s[4:5], vcc
	s_cbranch_execz .LBB0_741
	v_add_u32_e32 v2, s7, v0
	v_ashrrev_i32_e32 v3, 31, v2
	v_lshl_add_u64 v[2:3], v[2:3], 2, s[12:13]
	global_load_dword v16, v[2:3], off

.LBB0_746:
	s_lshl_b32 s4, s7, 2
	s_add_i32 s4, s4, 0
	s_add_i32 s4, s4, 0x20400
	v_mov_b32_e32 v4, s4
	ds_read2_b32 v[2:3], v4 offset1:32
	ds_read_b32 v4, v4 offset:384
	s_waitcnt lgkmcnt(1)
	v_readfirstlane_b32 s4, v3
	s_abs_i32 s4, s4
	s_nop 0
	v_cvt_f32_u32_e32 v3, s4
	v_readfirstlane_b32 s18, v2
	s_waitcnt lgkmcnt(0)
	v_readfirstlane_b32 s5, v4
	s_sub_i32 s14, 0, s4
	v_rcp_iflag_f32_e32 v3, v3
	s_lshl_b32 s5, s5, 4
	s_sub_i32 s5, s17, s5
	s_ashr_i32 s17, s5, 31
	v_mul_f32_e32 v2, 0x4f7ffffe, v3
	v_cvt_u32_f32_e32 v2, v2
	s_abs_i32 s5, s5
	v_readfirstlane_b32 s19, v2
	s_mul_i32 s14, s14, s19
	s_mul_hi_u32 s14, s19, s14
	s_add_i32 s19, s19, s14
	s_mul_hi_u32 s14, s5, s19
	s_mul_i32 s14, s14, s4
	s_sub_i32 s5, s5, s14
	s_sub_i32 s14, s5, s4
	s_cmp_ge_u32 s5, s4
	s_cselect_b32 s5, s14, s5
	s_sub_i32 s14, s5, s4
	s_cmp_ge_u32 s5, s4
	s_cselect_b32 s4, s14, s5
	s_xor_b32 s4, s4, s17
	s_sub_i32 s4, s4, s17
	s_lshl_b32 s5, s7, 13
	s_lshl_b32 s4, s4, 8
	s_add_i32 s14, s4, s5
	s_sub_i32 s4, s18, s4
	v_cmp_gt_i32_e32 vcc, s4, v0
	v_mov_b32_e32 v2, 0
	v_mov_b32_e32 v17, 0
	s_and_saveexec_b64 s[4:5], vcc
	s_cbranch_execz .LBB0_748
	v_add_u32_e32 v2, s14, v0
	v_ashrrev_i32_e32 v3, 31, v2
	v_lshl_add_u64 v[2:3], v[2:3], 2, s[12:13]
	global_load_dword v17, v[2:3], off

.LBB0_753:
	s_lshl_b32 s4, s14, 2
	s_add_i32 s4, s4, 0
	s_add_i32 s4, s4, 0x20400
	v_mov_b32_e32 v4, s4
	ds_read2_b32 v[2:3], v4 offset1:32
	ds_read_b32 v4, v4 offset:384
	s_waitcnt lgkmcnt(1)
	v_readfirstlane_b32 s4, v3
	s_abs_i32 s4, s4
	s_nop 0
	v_cvt_f32_u32_e32 v3, s4
	v_readfirstlane_b32 s18, v2
	s_waitcnt lgkmcnt(0)
	v_readfirstlane_b32 s5, v4
	s_sub_i32 s7, 0, s4
	v_rcp_iflag_f32_e32 v3, v3
	s_lshl_b32 s5, s5, 4
	s_sub_i32 s5, s17, s5
	s_ashr_i32 s17, s5, 31
	v_mul_f32_e32 v2, 0x4f7ffffe, v3
	v_cvt_u32_f32_e32 v2, v2
	s_abs_i32 s5, s5
	v_readfirstlane_b32 s19, v2
	s_mul_i32 s7, s7, s19
	s_mul_hi_u32 s7, s19, s7
	s_add_i32 s19, s19, s7
	s_mul_hi_u32 s7, s5, s19
	s_mul_i32 s7, s7, s4
	s_sub_i32 s5, s5, s7
	s_sub_i32 s7, s5, s4
	s_cmp_ge_u32 s5, s4
	s_cselect_b32 s5, s7, s5
	s_sub_i32 s7, s5, s4
	s_cmp_ge_u32 s5, s4
	s_cselect_b32 s4, s7, s5
	s_xor_b32 s4, s4, s17
	s_sub_i32 s4, s4, s17
	s_lshl_b32 s5, s14, 13
	s_lshl_b32 s4, s4, 8
	s_add_i32 s7, s4, s5
	s_sub_i32 s4, s18, s4
	v_cmp_gt_i32_e32 vcc, s4, v0
	v_mov_b32_e32 v2, 0
	v_mov_b32_e32 v18, 0
	s_and_saveexec_b64 s[4:5], vcc
	s_cbranch_execz .LBB0_755
	v_add_u32_e32 v2, s7, v0
	v_ashrrev_i32_e32 v3, 31, v2
	v_lshl_add_u64 v[2:3], v[2:3], 2, s[12:13]
	global_load_dword v18, v[2:3], off
.LBB0_755:
	s_or_b64 exec, exec, s[4:5]
	s_add_i32 s4, s15, s70
	s_cmp_ge_i32 s4, s48
	s_cbranch_scc1 .Lrt_fin
	s_ashr_i32 s5, s4, 31
	s_lshr_b32 s5, s5, 29
	s_add_i32 s5, s4, s5
	s_ashr_i32 s7, s5, 3
	s_and_b32 s5, s5, -8
	s_sub_i32 s4, s4, s5
	s_cmp_lt_i32 s4, 0
	s_cselect_b32 s2, s6, s2
	s_mul_i32 s2, s4, s2
	s_min_u32 s4, s16, 31
	s_lshl_b32 s4, s4, 2
	s_add_i32 s4, s4, 0
	s_add_i32 s2, s2, s7
	s_add_i32 s7, s4, 0x20584
	s_branch .LBB0_758

.LBB0_760:
	s_lshl_b32 s4, s6, 2
	s_add_i32 s4, s4, 0
	s_add_i32 s4, s4, 0x20400
	v_mov_b32_e32 v4, s4
	ds_read2_b32 v[2:3], v4 offset1:32
	ds_read_b32 v4, v4 offset:384
	s_waitcnt lgkmcnt(1)
	v_readfirstlane_b32 s4, v3
	s_abs_i32 s4, s4
	s_nop 0
	v_cvt_f32_u32_e32 v3, s4
	v_readfirstlane_b32 s7, v2
	s_waitcnt lgkmcnt(0)
	v_readfirstlane_b32 s5, v4
	s_lshl_b32 s5, s5, 4
	v_rcp_iflag_f32_e32 v3, v3
	s_sub_i32 s2, s2, s5
	s_sub_i32 s5, 0, s4
	s_ashr_i32 s14, s2, 31
	v_mul_f32_e32 v2, 0x4f7ffffe, v3
	v_cvt_u32_f32_e32 v2, v2
	s_abs_i32 s2, s2
	v_readfirstlane_b32 s15, v2
	s_mul_i32 s5, s5, s15
	s_mul_hi_u32 s5, s15, s5
	s_add_i32 s15, s15, s5
	s_mul_hi_u32 s5, s2, s15
	s_mul_i32 s5, s5, s4
	s_sub_i32 s2, s2, s5
	s_sub_i32 s5, s2, s4
	s_cmp_ge_u32 s2, s4
	s_cselect_b32 s2, s5, s2
	s_sub_i32 s5, s2, s4
	s_cmp_ge_u32 s2, s4
	s_cselect_b32 s2, s5, s2
	s_xor_b32 s2, s2, s14
	s_sub_i32 s2, s2, s14
	s_lshl_b32 s4, s6, 13
	s_lshl_b32 s5, s2, 8
	s_add_i32 s2, s5, s4
	s_sub_i32 s4, s7, s5
	v_cmp_gt_i32_e32 vcc, s4, v0
	v_mov_b32_e32 v2, 0
	v_mov_b32_e32 v19, 0
	s_and_saveexec_b64 s[4:5], vcc
	s_cbranch_execz .LBB0_762
	v_add_u32_e32 v2, s2, v0
	v_ashrrev_i32_e32 v3, 31, v2
	v_lshl_add_u64 v[2:3], v[2:3], 2, s[12:13]
	global_load_dword v19, v[2:3], off

.Lrt_fin:
	s_waitcnt vmcnt(0)
	v_ashrrev_i32_e32 v10, 2, v10
	ds_write_b32 v1, v10
	v_ashrrev_i32_e32 v11, 2, v11
	ds_write_b32 v1, v11 offset:1024
	v_ashrrev_i32_e32 v12, 2, v12
	ds_write_b32 v1, v12 offset:2048
	v_ashrrev_i32_e32 v13, 2, v13
	ds_write_b32 v1, v13 offset:3072
	v_ashrrev_i32_e32 v14, 2, v14
	ds_write_b32 v1, v14 offset:4096
	v_ashrrev_i32_e32 v15, 2, v15
	ds_write_b32 v1, v15 offset:5120
	v_ashrrev_i32_e32 v16, 2, v16
	ds_write_b32 v1, v16 offset:6144
	v_ashrrev_i32_e32 v17, 2, v17
	ds_write_b32 v1, v17 offset:7168
	v_ashrrev_i32_e32 v18, 2, v18
	ds_write_b32 v1, v18 offset:8192
	v_ashrrev_i32_e32 v19, 2, v19
	ds_write_b32 v1, v19 offset:9216
